# speedup vs baseline: 1.0089x; 1.0057x over previous
.LBB2_3:
	s_lshl_b32 s63, s53, 1
	s_add_i32 s61, s63, 2
	s_sub_i32 s2, s61, s40
	s_lshl_b32 s60, s53, 7
	s_min_i32 s62, s33, s2
	s_cmp_eq_u32 s55, 0
	s_cselect_b32 s79, s62, 0
	s_cmp_lt_i32 s2, 1
	s_waitcnt vmcnt(0)
	s_barrier
	s_cbranch_scc1 .LBB2_21
	s_add_i32 s63, s63, s55
	v_lshl_or_b32 v11, s63, 6, v83
	v_add_u32_e32 v10, s60, v82
	v_or_b32_e32 v12, 2, v11
	v_cmp_gt_i32_e64 s[6:7], v12, v10
	v_or_b32_e32 v12, 3, v11
	v_cmp_gt_i32_e64 s[8:9], v12, v10
	v_or_b32_e32 v12, 16, v11
	v_cmp_gt_i32_e64 s[10:11], v12, v10
	v_or_b32_e32 v12, 17, v11
	v_cmp_gt_i32_e64 s[12:13], v12, v10
	v_or_b32_e32 v12, 18, v11
	v_cmp_gt_i32_e64 s[14:15], v12, v10
	v_or_b32_e32 v12, 19, v11
	v_cmp_gt_i32_e64 s[16:17], v12, v10
	v_or_b32_e32 v12, 32, v11
	v_cmp_gt_i32_e64 s[18:19], v12, v10
	v_or_b32_e32 v12, 33, v11
	v_cmp_gt_i32_e64 s[20:21], v12, v10
	v_or_b32_e32 v12, 34, v11
	v_cmp_gt_i32_e64 s[22:23], v12, v10
	v_or_b32_e32 v12, 35, v11
	v_cmp_gt_i32_e64 s[24:25], v12, v10
	v_or_b32_e32 v12, 48, v11
	s_sub_i32 s37, s56, s40
	v_cmp_gt_i32_e64 s[26:27], v12, v10
	v_or_b32_e32 v12, 49, v11
	s_min_i32 s37, s33, s37
	v_cmp_gt_i32_e64 s[2:3], v11, v10
	v_cmp_lt_i32_e64 s[4:5], v11, v10
	v_cmp_gt_i32_e64 s[28:29], v12, v10
	v_or_b32_e32 v12, 50, v11
	v_or_b32_e32 v11, 51, v11
	s_max_i32 s37, s37, 1
	s_lshl_b64 s[38:39], s[40:41], 13
	v_mov_b32_e32 v67, 0
	v_cmp_gt_i32_e64 s[30:31], v12, v10
	v_cmp_gt_i32_e64 s[34:35], v11, v10
	s_mov_b32 s64, 1
	s_sub_i32 s65, 0, s37
	s_add_i32 s66, s40, s57
	s_add_u32 s68, s70, s38
	s_addc_u32 s69, s71, s39
	s_add_u32 s74, s72, s38
	s_addc_u32 s75, s73, s39
	v_mov_b32_e32 v14, v51
	v_mov_b32_e32 v15, v51
	v_mov_b32_e32 v16, v51
	v_mov_b32_e32 v17, v51
	s_mov_b64 s[38:39], -1
	v_mov_b32_e32 v30, 0
	v_mov_b32_e32 v31, v67
	v_mov_b32_e32 v32, v67
	v_mov_b32_e32 v33, v67
	v_mov_b32_e32 v26, 0
	v_mov_b32_e32 v27, v67
	v_mov_b32_e32 v28, v67
	v_mov_b32_e32 v29, v67
	v_mov_b32_e32 v22, v67
	v_mov_b32_e32 v23, v67
	v_mov_b32_e32 v24, v67
	v_mov_b32_e32 v25, v67
	v_mov_b32_e32 v18, v67
	v_mov_b32_e32 v19, v67
	v_mov_b32_e32 v20, v67
	v_mov_b32_e32 v21, v67
	v_mov_b32_e32 v10, v67
	v_mov_b32_e32 v11, v67
	v_mov_b32_e32 v12, v67
	v_mov_b32_e32 v13, v67
	s_mov_b32 s37, 0
	s_mov_b32 s80, 0
	s_mov_b32 s81, 0
	s_mov_b32 s48, s40
	v_mov_b32_e32 v114, v57
	v_mov_b32_e32 v115, v81
	v_mov_b32_e32 v120, v57
	v_mov_b32_e32 v121, v81
	s_cmp_gt_u32 s48, s63
	s_branch .Lattn_after_rdv

.Lattn_skip_tile:
	s_cmp_lt_i32 s64, s79
	s_cbranch_scc0 .LBB2_6
	s_add_i32 s48, s37, 0x4000
	s_cmp_eq_u32 s48, 0xc000
	s_cselect_b32 s48, 0, s48
	s_add_i32 s48, s78, s48
	s_mov_b32 m0, s48
	s_nop 0
	global_load_lds_dwordx4 v64, s[68:69]
	s_add_i32 m0, s48, 0x400
	s_nop 0
	global_load_lds_dwordx4 v65, s[68:69]
	s_add_i32 m0, s48, 0x2000
	s_nop 0
	global_load_lds_dwordx4 v64, s[74:75]
	s_add_i32 m0, s48, 0x2400
	s_nop 0
	global_load_lds_dwordx4 v65, s[74:75]
	s_branch .LBB2_6
